# combo + loop-edge rotation: K-loop counter and pointer updates moved in front of the last barrier in the five GEMM loops
# baseline (speedup 1.0000x reference)
.LBB0_200:
	s_add_u32 s72, s42, 0xfff80000
	s_addc_u32 s73, s43, -1
	s_mov_b32 m0, s57
	s_nop 0
	global_load_lds_dwordx4 v160, s[72:73]
	s_mov_b32 m0, s58
	s_nop 0
	global_load_lds_dwordx4 v164, s[72:73]
	ds_read_b128 v[16:19], v186
	ds_read_b128 v[20:23], v187
	ds_read_b128 v[24:27], v188
	ds_read_b128 v[28:31], v189
	ds_read_b128 v[0:3], v190
	ds_read_b128 v[4:7], v191
	ds_read_b128 v[8:11], v192
	ds_read_b128 v[12:15], v193
	s_add_u32 s44, s42, 0xfff80080
	s_addc_u32 s45, s43, -1
	s_cmp_eq_u32 s68, 28
	s_cselect_b32 s47, s31, s45
	s_cselect_b32 s46, s35, s44
	s_cselect_b32 s45, s29, s67
	s_cselect_b32 s44, s39, s66
	s_add_i32 m0, s27, 0xc000
	ds_read_b128 v[178:181], v218
	ds_read_b128 v[182:185], v218 offset:1024
	ds_read_b128 v[222:225], v218 offset:2048
	ds_read_b128 v[226:229], v218 offset:3072
	ds_read_b128 v[230:233], v218 offset:4096
	ds_read_b128 v[234:237], v218 offset:5120
	ds_read_b128 v[238:241], v218 offset:6144
	ds_read_b128 v[242:245], v218 offset:7168
	global_load_lds_dwordx4 v172, s[42:43]
	s_add_i32 m0, s27, 0xe000
	s_nop 0
	global_load_lds_dwordx4 v174, s[42:43]
	s_waitcnt vmcnt(8)
	s_waitcnt lgkmcnt(0)
	s_barrier
	s_setprio 1
	s_waitcnt lgkmcnt(0)
	v_mfma_f32_16x16x128_f8f6f4 v[156:159], v[16:23], v[178:185], v[156:159]
	v_mfma_f32_16x16x128_f8f6f4 v[152:155], v[24:31], v[178:185], v[152:155]
	v_mfma_f32_16x16x128_f8f6f4 v[148:151], v[16:23], v[222:229], v[148:151]
	v_mfma_f32_16x16x128_f8f6f4 v[144:147], v[24:31], v[222:229], v[144:147]
	v_mfma_f32_16x16x128_f8f6f4 v[140:143], v[16:23], v[230:237], v[140:143]
	v_mfma_f32_16x16x128_f8f6f4 v[136:139], v[24:31], v[230:237], v[136:139]
	v_mfma_f32_16x16x128_f8f6f4 v[132:135], v[16:23], v[238:245], v[132:135]
	v_mfma_f32_16x16x128_f8f6f4 v[128:131], v[24:31], v[238:245], v[128:131]
	s_setprio 0
	s_setprio 1
	v_mfma_f32_16x16x128_f8f6f4 v[124:127], v[0:7], v[178:185], v[124:127]
	v_mfma_f32_16x16x128_f8f6f4 v[120:123], v[8:15], v[178:185], v[120:123]
	v_mfma_f32_16x16x128_f8f6f4 v[116:119], v[0:7], v[222:229], v[116:119]
	v_mfma_f32_16x16x128_f8f6f4 v[112:115], v[8:15], v[222:229], v[112:115]
	v_mfma_f32_16x16x128_f8f6f4 v[108:111], v[0:7], v[230:237], v[108:111]
	v_mfma_f32_16x16x128_f8f6f4 v[104:107], v[8:15], v[230:237], v[104:107]
	v_mfma_f32_16x16x128_f8f6f4 v[100:103], v[0:7], v[238:245], v[100:103]
	v_mfma_f32_16x16x128_f8f6f4 v[96:99], v[8:15], v[238:245], v[96:99]
	s_setprio 0
	s_barrier
	s_mov_b32 m0, s33
	v_lshl_add_u64 v[178:179], s[44:45], 0, v[162:163]
	s_add_u32 s70, s44, 0x80000
	ds_read_b128 v[222:225], v218 offset:16384
	ds_read_b128 v[226:229], v218 offset:17408
	ds_read_b128 v[230:233], v218 offset:18432
	ds_read_b128 v[234:237], v218 offset:19456
	ds_read_b128 v[238:241], v218 offset:20480
	ds_read_b128 v[242:245], v218 offset:21504
	ds_read_b128 v[246:249], v218 offset:22528
	ds_read_b128 v[250:253], v218 offset:23552
	global_load_lds_dwordx4 v[178:179], off
	v_lshl_add_u64 v[180:181], s[44:45], 0, v[166:167]
	s_mov_b32 m0, s48
	s_addc_u32 s71, s45, 0
	global_load_lds_dwordx4 v[180:181], off
	s_mov_b32 m0, s49
	s_nop 0
	global_load_lds_dwordx4 v162, s[70:71]
	s_mov_b32 m0, s50
	s_nop 0
	global_load_lds_dwordx4 v166, s[70:71]
	s_waitcnt vmcnt(6)
	s_waitcnt lgkmcnt(0)
	s_barrier
	s_setprio 1
	s_waitcnt lgkmcnt(0)
	v_mfma_f32_16x16x128_f8f6f4 v[92:95], v[16:23], v[222:229], v[92:95]
	v_mfma_f32_16x16x128_f8f6f4 v[88:91], v[24:31], v[222:229], v[88:91]
	v_mfma_f32_16x16x128_f8f6f4 v[84:87], v[16:23], v[230:237], v[84:87]
	v_mfma_f32_16x16x128_f8f6f4 v[80:83], v[24:31], v[230:237], v[80:83]
	v_mfma_f32_16x16x128_f8f6f4 v[76:79], v[16:23], v[238:245], v[76:79]
	v_mfma_f32_16x16x128_f8f6f4 v[72:75], v[24:31], v[238:245], v[72:75]
	v_mfma_f32_16x16x128_f8f6f4 v[68:71], v[16:23], v[246:253], v[68:71]
	v_mfma_f32_16x16x128_f8f6f4 v[64:67], v[24:31], v[246:253], v[64:67]
	s_setprio 0
	s_setprio 1
	v_mfma_f32_16x16x128_f8f6f4 v[60:63], v[0:7], v[222:229], v[60:63]
	v_mfma_f32_16x16x128_f8f6f4 v[56:59], v[8:15], v[222:229], v[56:59]
	v_mfma_f32_16x16x128_f8f6f4 v[52:55], v[0:7], v[230:237], v[52:55]
	v_mfma_f32_16x16x128_f8f6f4 v[48:51], v[8:15], v[230:237], v[48:51]
	v_mfma_f32_16x16x128_f8f6f4 v[44:47], v[0:7], v[238:245], v[44:47]
	v_mfma_f32_16x16x128_f8f6f4 v[40:43], v[8:15], v[238:245], v[40:43]
	v_mfma_f32_16x16x128_f8f6f4 v[36:39], v[0:7], v[246:253], v[36:39]
	v_mfma_f32_16x16x128_f8f6f4 v[32:35], v[8:15], v[246:253], v[32:35]
	s_setprio 0
	s_barrier
	s_mov_b32 m0, s27
	s_nop 0
	global_load_lds_dwordx4 v160, s[46:47]
	s_mov_b32 m0, s51
	s_nop 0
	global_load_lds_dwordx4 v164, s[46:47]
	ds_read_b128 v[0:3], v194
	ds_read_b128 v[4:7], v195
	ds_read_b128 v[8:11], v196
	ds_read_b128 v[12:15], v197
	ds_read_b128 v[16:19], v198
	ds_read_b128 v[20:23], v199
	ds_read_b128 v[24:27], v200
	ds_read_b128 v[28:31], v201
	s_add_u32 s46, s46, 0x80000
	s_addc_u32 s47, s47, 0
	s_mov_b32 m0, s52
	ds_read_b128 v[222:225], v218 offset:32768
	ds_read_b128 v[226:229], v218 offset:33792
	ds_read_b128 v[230:233], v218 offset:34816
	ds_read_b128 v[234:237], v218 offset:35840
	ds_read_b128 v[238:241], v218 offset:36864
	ds_read_b128 v[242:245], v218 offset:37888
	ds_read_b128 v[246:249], v218 offset:38912
	ds_read_b128 v[250:253], v218 offset:39936
	global_load_lds_dwordx4 v160, s[46:47]
	s_mov_b32 m0, s53
	s_nop 0
	global_load_lds_dwordx4 v164, s[46:47]
	s_waitcnt vmcnt(8)
	s_waitcnt lgkmcnt(0)
	s_barrier
	s_setprio 1
	s_waitcnt lgkmcnt(0)
	v_mfma_f32_16x16x128_f8f6f4 v[156:159], v[0:7], v[222:229], v[156:159]
	v_mfma_f32_16x16x128_f8f6f4 v[152:155], v[8:15], v[222:229], v[152:155]
	v_mfma_f32_16x16x128_f8f6f4 v[148:151], v[0:7], v[230:237], v[148:151]
	v_mfma_f32_16x16x128_f8f6f4 v[144:147], v[8:15], v[230:237], v[144:147]
	v_mfma_f32_16x16x128_f8f6f4 v[140:143], v[0:7], v[238:245], v[140:143]
	v_mfma_f32_16x16x128_f8f6f4 v[136:139], v[8:15], v[238:245], v[136:139]
	v_mfma_f32_16x16x128_f8f6f4 v[132:135], v[0:7], v[246:253], v[132:135]
	v_mfma_f32_16x16x128_f8f6f4 v[128:131], v[8:15], v[246:253], v[128:131]
	s_setprio 0
	s_setprio 1
	v_mfma_f32_16x16x128_f8f6f4 v[124:127], v[16:23], v[222:229], v[124:127]
	v_mfma_f32_16x16x128_f8f6f4 v[120:123], v[24:31], v[222:229], v[120:123]
	v_mfma_f32_16x16x128_f8f6f4 v[116:119], v[16:23], v[230:237], v[116:119]
	v_mfma_f32_16x16x128_f8f6f4 v[112:115], v[24:31], v[230:237], v[112:115]
	v_mfma_f32_16x16x128_f8f6f4 v[108:111], v[16:23], v[238:245], v[108:111]
	v_mfma_f32_16x16x128_f8f6f4 v[104:107], v[24:31], v[238:245], v[104:107]
	v_mfma_f32_16x16x128_f8f6f4 v[100:103], v[16:23], v[246:253], v[100:103]
	v_mfma_f32_16x16x128_f8f6f4 v[96:99], v[24:31], v[246:253], v[96:99]
	s_setprio 0
	s_barrier
	s_mov_b32 m0, s55
	v_lshl_add_u64 v[176:177], v[178:179], 0, s[20:21]
	s_add_u32 s44, s44, 0x80080
	ds_read_b128 v[222:225], v218 offset:49152
	ds_read_b128 v[226:229], v218 offset:50176
	ds_read_b128 v[230:233], v218 offset:51200
	ds_read_b128 v[234:237], v218 offset:52224
	ds_read_b128 v[238:241], v218 offset:53248
	ds_read_b128 v[242:245], v218 offset:54272
	ds_read_b128 v[246:249], v218 offset:55296
	ds_read_b128 v[250:253], v218 offset:56320
	global_load_lds_dwordx4 v[176:177], off
	v_lshl_add_u64 v[176:177], v[180:181], 0, s[20:21]
	s_mov_b32 m0, s56
	s_addc_u32 s45, s45, 0
	global_load_lds_dwordx4 v[176:177], off
	s_mov_b32 m0, s59
	s_nop 0
	global_load_lds_dwordx4 v162, s[44:45]
	s_mov_b32 m0, s60
	s_nop 0
	global_load_lds_dwordx4 v166, s[44:45]
	s_waitcnt vmcnt(6)
	s_waitcnt lgkmcnt(0)
	s_barrier
	s_setprio 1
	s_waitcnt lgkmcnt(0)
	v_mfma_f32_16x16x128_f8f6f4 v[92:95], v[0:7], v[222:229], v[92:95]
	v_mfma_f32_16x16x128_f8f6f4 v[88:91], v[8:15], v[222:229], v[88:91]
	v_mfma_f32_16x16x128_f8f6f4 v[84:87], v[0:7], v[230:237], v[84:87]
	v_mfma_f32_16x16x128_f8f6f4 v[80:83], v[8:15], v[230:237], v[80:83]
	v_mfma_f32_16x16x128_f8f6f4 v[76:79], v[0:7], v[238:245], v[76:79]
	v_mfma_f32_16x16x128_f8f6f4 v[72:75], v[8:15], v[238:245], v[72:75]
	v_mfma_f32_16x16x128_f8f6f4 v[68:71], v[0:7], v[246:253], v[68:71]
	v_mfma_f32_16x16x128_f8f6f4 v[64:67], v[8:15], v[246:253], v[64:67]
	s_setprio 0
	s_setprio 1
	v_mfma_f32_16x16x128_f8f6f4 v[60:63], v[16:23], v[222:229], v[60:63]
	v_mfma_f32_16x16x128_f8f6f4 v[56:59], v[24:31], v[222:229], v[56:59]
	v_mfma_f32_16x16x128_f8f6f4 v[52:55], v[16:23], v[230:237], v[52:55]
	v_mfma_f32_16x16x128_f8f6f4 v[48:51], v[24:31], v[230:237], v[48:51]
	v_mfma_f32_16x16x128_f8f6f4 v[44:47], v[16:23], v[238:245], v[44:47]
	v_mfma_f32_16x16x128_f8f6f4 v[40:43], v[24:31], v[238:245], v[40:43]
	v_mfma_f32_16x16x128_f8f6f4 v[36:39], v[16:23], v[246:253], v[36:39]
	v_mfma_f32_16x16x128_f8f6f4 v[32:35], v[24:31], v[246:253], v[32:35]
	s_add_i32 s68, s68, 2
	s_add_u32 s42, s42, 0x100
	s_addc_u32 s43, s43, 0
	s_add_u32 s66, s66, 0x100
	s_addc_u32 s67, s67, 0
	s_setprio 0
	s_barrier
	s_cmp_gt_u32 s68, 29
	s_cbranch_scc0 .LBB0_200
	s_nop 15
	s_nop 15
	s_and_b64 vcc, exec, s[22:23]
	s_cbranch_vccz .LBB0_203
	s_barrier

.LBB0_562:
	s_add_u32 s72, s30, 0xfff80000
	s_addc_u32 s73, s31, -1
	s_mov_b32 m0, s49
	s_nop 0
	global_load_lds_dwordx4 v160, s[72:73]
	s_mov_b32 m0, s50
	s_nop 0
	global_load_lds_dwordx4 v162, s[72:73]
	ds_read_b128 v[16:19], v181
	ds_read_b128 v[20:23], v182
	ds_read_b128 v[24:27], v183
	ds_read_b128 v[28:31], v184
	ds_read_b128 v[0:3], v185
	ds_read_b128 v[4:7], v186
	ds_read_b128 v[8:11], v187
	ds_read_b128 v[12:15], v188
	s_add_u32 s34, s30, 0xfff80080
	s_addc_u32 s35, s31, -1
	s_cmp_eq_u32 s59, 28
	s_cselect_b32 s37, s23, s35
	s_cselect_b32 s36, s55, s34
	s_cselect_b32 s35, s21, s58
	s_cselect_b32 s34, s56, s57
	s_add_i32 m0, s29, 0xc000
	ds_read_b128 v[172:175], v198
	ds_read_b128 v[176:179], v198 offset:1024
	ds_read_b128 v[200:203], v198 offset:2048
	ds_read_b128 v[204:207], v198 offset:3072
	ds_read_b128 v[208:211], v198 offset:4096
	ds_read_b128 v[212:215], v198 offset:5120
	ds_read_b128 v[216:219], v198 offset:6144
	ds_read_b128 v[220:223], v198 offset:7168
	global_load_lds_dwordx4 v164, s[30:31]
	s_add_i32 m0, s29, 0xe000
	s_nop 0
	global_load_lds_dwordx4 v166, s[30:31]
	s_waitcnt vmcnt(8)
	s_waitcnt lgkmcnt(0)
	s_barrier
	s_setprio 1
	s_waitcnt lgkmcnt(0)
	v_mfma_f32_16x16x128_f8f6f4 v[156:159], v[16:23], v[172:179], v[156:159]
	v_mfma_f32_16x16x128_f8f6f4 v[152:155], v[24:31], v[172:179], v[152:155]
	v_mfma_f32_16x16x128_f8f6f4 v[148:151], v[16:23], v[200:207], v[148:151]
	v_mfma_f32_16x16x128_f8f6f4 v[144:147], v[24:31], v[200:207], v[144:147]
	v_mfma_f32_16x16x128_f8f6f4 v[124:127], v[16:23], v[208:215], v[124:127]
	v_mfma_f32_16x16x128_f8f6f4 v[120:123], v[24:31], v[208:215], v[120:123]
	v_mfma_f32_16x16x128_f8f6f4 v[116:119], v[16:23], v[216:223], v[116:119]
	v_mfma_f32_16x16x128_f8f6f4 v[112:115], v[24:31], v[216:223], v[112:115]
	s_setprio 0
	s_setprio 1
	v_mfma_f32_16x16x128_f8f6f4 v[140:143], v[0:7], v[172:179], v[140:143]
	v_mfma_f32_16x16x128_f8f6f4 v[136:139], v[8:15], v[172:179], v[136:139]
	v_mfma_f32_16x16x128_f8f6f4 v[132:135], v[0:7], v[200:207], v[132:135]
	v_mfma_f32_16x16x128_f8f6f4 v[128:131], v[8:15], v[200:207], v[128:131]
	v_mfma_f32_16x16x128_f8f6f4 v[108:111], v[0:7], v[208:215], v[108:111]
	v_mfma_f32_16x16x128_f8f6f4 v[104:107], v[8:15], v[208:215], v[104:107]
	v_mfma_f32_16x16x128_f8f6f4 v[100:103], v[0:7], v[216:223], v[100:103]
	v_mfma_f32_16x16x128_f8f6f4 v[96:99], v[8:15], v[216:223], v[96:99]
	s_setprio 0
	s_barrier
	s_mov_b32 m0, s33
	v_lshl_add_u64 v[172:173], s[34:35], 0, v[160:161]
	s_add_u32 s60, s34, 0x80000
	ds_read_b128 v[200:203], v198 offset:16384
	ds_read_b128 v[204:207], v198 offset:17408
	ds_read_b128 v[208:211], v198 offset:18432
	ds_read_b128 v[212:215], v198 offset:19456
	ds_read_b128 v[216:219], v198 offset:20480
	ds_read_b128 v[220:223], v198 offset:21504
	ds_read_b128 v[224:227], v198 offset:22528
	ds_read_b128 v[228:231], v198 offset:23552
	global_load_lds_dwordx4 v[172:173], off
	v_lshl_add_u64 v[174:175], s[34:35], 0, v[162:163]
	s_mov_b32 m0, s38
	s_addc_u32 s61, s35, 0
	global_load_lds_dwordx4 v[174:175], off
	s_mov_b32 m0, s39
	s_nop 0
	global_load_lds_dwordx4 v160, s[60:61]
	s_mov_b32 m0, s40
	s_nop 0
	global_load_lds_dwordx4 v162, s[60:61]
	s_waitcnt vmcnt(6)
	s_waitcnt lgkmcnt(0)
	s_barrier
	s_setprio 1
	s_waitcnt lgkmcnt(0)
	v_mfma_f32_16x16x128_f8f6f4 v[92:95], v[16:23], v[200:207], v[92:95]
	v_mfma_f32_16x16x128_f8f6f4 v[88:91], v[24:31], v[200:207], v[88:91]
	v_mfma_f32_16x16x128_f8f6f4 v[84:87], v[16:23], v[208:215], v[84:87]
	v_mfma_f32_16x16x128_f8f6f4 v[80:83], v[24:31], v[208:215], v[80:83]
	v_mfma_f32_16x16x128_f8f6f4 v[60:63], v[16:23], v[216:223], v[60:63]
	v_mfma_f32_16x16x128_f8f6f4 v[56:59], v[24:31], v[216:223], v[56:59]
	v_mfma_f32_16x16x128_f8f6f4 v[52:55], v[16:23], v[224:231], v[52:55]
	v_mfma_f32_16x16x128_f8f6f4 v[48:51], v[24:31], v[224:231], v[48:51]
	s_setprio 0
	s_setprio 1
	v_mfma_f32_16x16x128_f8f6f4 v[76:79], v[0:7], v[200:207], v[76:79]
	v_mfma_f32_16x16x128_f8f6f4 v[72:75], v[8:15], v[200:207], v[72:75]
	v_mfma_f32_16x16x128_f8f6f4 v[68:71], v[0:7], v[208:215], v[68:71]
	v_mfma_f32_16x16x128_f8f6f4 v[64:67], v[8:15], v[208:215], v[64:67]
	v_mfma_f32_16x16x128_f8f6f4 v[44:47], v[0:7], v[216:223], v[44:47]
	v_mfma_f32_16x16x128_f8f6f4 v[40:43], v[8:15], v[216:223], v[40:43]
	v_mfma_f32_16x16x128_f8f6f4 v[36:39], v[0:7], v[224:231], v[36:39]
	v_mfma_f32_16x16x128_f8f6f4 v[32:35], v[8:15], v[224:231], v[32:35]
	s_setprio 0
	s_barrier
	s_mov_b32 m0, s29
	s_nop 0
	global_load_lds_dwordx4 v160, s[36:37]
	s_mov_b32 m0, s41
	s_nop 0
	global_load_lds_dwordx4 v162, s[36:37]
	ds_read_b128 v[0:3], v189
	ds_read_b128 v[4:7], v190
	ds_read_b128 v[8:11], v191
	ds_read_b128 v[12:15], v192
	ds_read_b128 v[16:19], v193
	ds_read_b128 v[20:23], v194
	ds_read_b128 v[24:27], v195
	ds_read_b128 v[28:31], v196
	s_add_u32 s36, s36, 0x80000
	s_addc_u32 s37, s37, 0
	s_mov_b32 m0, s42
	ds_read_b128 v[200:203], v198 offset:32768
	ds_read_b128 v[204:207], v198 offset:33792
	ds_read_b128 v[208:211], v198 offset:34816
	ds_read_b128 v[212:215], v198 offset:35840
	ds_read_b128 v[216:219], v198 offset:36864
	ds_read_b128 v[220:223], v198 offset:37888
	ds_read_b128 v[224:227], v198 offset:38912
	ds_read_b128 v[228:231], v198 offset:39936
	global_load_lds_dwordx4 v160, s[36:37]
	s_mov_b32 m0, s43
	s_nop 0
	global_load_lds_dwordx4 v162, s[36:37]
	s_waitcnt vmcnt(8)
	s_waitcnt lgkmcnt(0)
	s_barrier
	s_setprio 1
	s_waitcnt lgkmcnt(0)
	v_mfma_f32_16x16x128_f8f6f4 v[156:159], v[0:7], v[200:207], v[156:159]
	v_mfma_f32_16x16x128_f8f6f4 v[152:155], v[8:15], v[200:207], v[152:155]
	v_mfma_f32_16x16x128_f8f6f4 v[148:151], v[0:7], v[208:215], v[148:151]
	v_mfma_f32_16x16x128_f8f6f4 v[144:147], v[8:15], v[208:215], v[144:147]
	v_mfma_f32_16x16x128_f8f6f4 v[124:127], v[0:7], v[216:223], v[124:127]
	v_mfma_f32_16x16x128_f8f6f4 v[120:123], v[8:15], v[216:223], v[120:123]
	v_mfma_f32_16x16x128_f8f6f4 v[116:119], v[0:7], v[224:231], v[116:119]
	v_mfma_f32_16x16x128_f8f6f4 v[112:115], v[8:15], v[224:231], v[112:115]
	s_setprio 0
	s_setprio 1
	v_mfma_f32_16x16x128_f8f6f4 v[140:143], v[16:23], v[200:207], v[140:143]
	v_mfma_f32_16x16x128_f8f6f4 v[136:139], v[24:31], v[200:207], v[136:139]
	v_mfma_f32_16x16x128_f8f6f4 v[132:135], v[16:23], v[208:215], v[132:135]
	v_mfma_f32_16x16x128_f8f6f4 v[128:131], v[24:31], v[208:215], v[128:131]
	v_mfma_f32_16x16x128_f8f6f4 v[108:111], v[16:23], v[216:223], v[108:111]
	v_mfma_f32_16x16x128_f8f6f4 v[104:107], v[24:31], v[216:223], v[104:107]
	v_mfma_f32_16x16x128_f8f6f4 v[100:103], v[16:23], v[224:231], v[100:103]
	v_mfma_f32_16x16x128_f8f6f4 v[96:99], v[24:31], v[224:231], v[96:99]
	s_setprio 0
	s_barrier
	s_mov_b32 m0, s47
	v_lshl_add_u64 v[172:173], v[172:173], 0, s[14:15]
	s_add_u32 s34, s34, 0x80080
	ds_read_b128 v[200:203], v198 offset:49152
	ds_read_b128 v[204:207], v198 offset:50176
	ds_read_b128 v[208:211], v198 offset:51200
	ds_read_b128 v[212:215], v198 offset:52224
	ds_read_b128 v[216:219], v198 offset:53248
	ds_read_b128 v[220:223], v198 offset:54272
	ds_read_b128 v[224:227], v198 offset:55296
	ds_read_b128 v[228:231], v198 offset:56320
	global_load_lds_dwordx4 v[172:173], off
	v_lshl_add_u64 v[172:173], v[174:175], 0, s[14:15]
	s_mov_b32 m0, s48
	s_addc_u32 s35, s35, 0
	global_load_lds_dwordx4 v[172:173], off
	s_mov_b32 m0, s51
	s_nop 0
	global_load_lds_dwordx4 v160, s[34:35]
	s_mov_b32 m0, s52
	s_nop 0
	global_load_lds_dwordx4 v162, s[34:35]
	s_waitcnt vmcnt(6)
	s_waitcnt lgkmcnt(0)
	s_barrier
	s_setprio 1
	s_waitcnt lgkmcnt(0)
	v_mfma_f32_16x16x128_f8f6f4 v[92:95], v[0:7], v[200:207], v[92:95]
	v_mfma_f32_16x16x128_f8f6f4 v[88:91], v[8:15], v[200:207], v[88:91]
	v_mfma_f32_16x16x128_f8f6f4 v[84:87], v[0:7], v[208:215], v[84:87]
	v_mfma_f32_16x16x128_f8f6f4 v[80:83], v[8:15], v[208:215], v[80:83]
	v_mfma_f32_16x16x128_f8f6f4 v[60:63], v[0:7], v[216:223], v[60:63]
	v_mfma_f32_16x16x128_f8f6f4 v[56:59], v[8:15], v[216:223], v[56:59]
	v_mfma_f32_16x16x128_f8f6f4 v[52:55], v[0:7], v[224:231], v[52:55]
	v_mfma_f32_16x16x128_f8f6f4 v[48:51], v[8:15], v[224:231], v[48:51]
	s_setprio 0
	s_setprio 1
	v_mfma_f32_16x16x128_f8f6f4 v[76:79], v[16:23], v[200:207], v[76:79]
	v_mfma_f32_16x16x128_f8f6f4 v[72:75], v[24:31], v[200:207], v[72:75]
	v_mfma_f32_16x16x128_f8f6f4 v[68:71], v[16:23], v[208:215], v[68:71]
	v_mfma_f32_16x16x128_f8f6f4 v[64:67], v[24:31], v[208:215], v[64:67]
	v_mfma_f32_16x16x128_f8f6f4 v[44:47], v[16:23], v[216:223], v[44:47]
	v_mfma_f32_16x16x128_f8f6f4 v[40:43], v[24:31], v[216:223], v[40:43]
	v_mfma_f32_16x16x128_f8f6f4 v[36:39], v[16:23], v[224:231], v[36:39]
	v_mfma_f32_16x16x128_f8f6f4 v[32:35], v[24:31], v[224:231], v[32:35]
	s_add_i32 s59, s59, 2
	s_add_u32 s30, s30, 0x100
	s_addc_u32 s31, s31, 0
	s_add_u32 s57, s57, 0x100
	s_addc_u32 s58, s58, 0
	s_setprio 0
	s_barrier
	s_cmp_gt_u32 s59, 29
	s_cbranch_scc0 .LBB0_562
	s_nop 15
	s_nop 15
	s_and_b64 vcc, exec, s[16:17]
	s_cbranch_vccz .LBB0_565
	s_barrier

.LBB0_687:
	s_add_u32 s72, s24, 0xfff00000
	s_addc_u32 s73, s25, -1
	s_mov_b32 m0, s44
	s_nop 0
	global_load_lds_dwordx4 v128, s[72:73]
	s_mov_b32 m0, s45
	s_nop 0
	global_load_lds_dwordx4 v130, s[72:73]
	ds_read_b128 v[160:163], v142
	ds_read_b128 v[164:167], v143
	ds_read_b128 v[168:171], v144
	ds_read_b128 v[172:175], v145
	ds_read_b128 v[176:179], v146
	ds_read_b128 v[180:183], v147
	ds_read_b128 v[184:187], v148
	ds_read_b128 v[188:191], v149
	s_add_u32 s26, s24, 0xfff00080
	s_addc_u32 s27, s25, -1
	s_cmp_eq_u32 s54, 60
	s_cselect_b32 s29, s19, s27
	s_cselect_b32 s28, s50, s26
	s_cselect_b32 s27, s17, s53
	s_cselect_b32 s26, s51, s52
	s_add_i32 m0, s33, 0xc000
	ds_read_b128 v[192:195], v158
	ds_read_b128 v[196:199], v158 offset:1024
	ds_read_b128 v[200:203], v158 offset:2048
	ds_read_b128 v[204:207], v158 offset:3072
	ds_read_b128 v[208:211], v158 offset:4096
	ds_read_b128 v[212:215], v158 offset:5120
	ds_read_b128 v[216:219], v158 offset:6144
	ds_read_b128 v[220:223], v158 offset:7168
	global_load_lds_dwordx4 v134, s[24:25]
	s_add_i32 m0, s33, 0xe000
	s_nop 0
	global_load_lds_dwordx4 v136, s[24:25]
	s_waitcnt vmcnt(8)
	s_waitcnt lgkmcnt(0)
	s_barrier
	s_setprio 1
	s_waitcnt lgkmcnt(0)
	v_mfma_f32_16x16x32_bf16 v[124:127], v[160:163], v[192:195], v[124:127]
	v_mfma_f32_16x16x32_bf16 v[120:123], v[168:171], v[192:195], v[120:123]
	v_mfma_f32_16x16x32_bf16 v[116:119], v[160:163], v[200:203], v[116:119]
	v_mfma_f32_16x16x32_bf16 v[112:115], v[168:171], v[200:203], v[112:115]
	v_mfma_f32_16x16x32_bf16 v[108:111], v[160:163], v[208:211], v[108:111]
	v_mfma_f32_16x16x32_bf16 v[104:107], v[168:171], v[208:211], v[104:107]
	v_mfma_f32_16x16x32_bf16 v[100:103], v[160:163], v[216:219], v[100:103]
	v_mfma_f32_16x16x32_bf16 v[96:99], v[168:171], v[216:219], v[96:99]
	v_mfma_f32_16x16x32_bf16 v[124:127], v[164:167], v[196:199], v[124:127]
	v_mfma_f32_16x16x32_bf16 v[120:123], v[172:175], v[196:199], v[120:123]
	v_mfma_f32_16x16x32_bf16 v[116:119], v[164:167], v[204:207], v[116:119]
	v_mfma_f32_16x16x32_bf16 v[112:115], v[172:175], v[204:207], v[112:115]
	v_mfma_f32_16x16x32_bf16 v[108:111], v[164:167], v[212:215], v[108:111]
	v_mfma_f32_16x16x32_bf16 v[104:107], v[172:175], v[212:215], v[104:107]
	v_mfma_f32_16x16x32_bf16 v[100:103], v[164:167], v[220:223], v[100:103]
	v_mfma_f32_16x16x32_bf16 v[96:99], v[172:175], v[220:223], v[96:99]
	s_setprio 0
	s_setprio 1
	v_mfma_f32_16x16x32_bf16 v[92:95], v[176:179], v[192:195], v[92:95]
	v_mfma_f32_16x16x32_bf16 v[88:91], v[184:187], v[192:195], v[88:91]
	v_mfma_f32_16x16x32_bf16 v[84:87], v[176:179], v[200:203], v[84:87]
	v_mfma_f32_16x16x32_bf16 v[80:83], v[184:187], v[200:203], v[80:83]
	v_mfma_f32_16x16x32_bf16 v[76:79], v[176:179], v[208:211], v[76:79]
	v_mfma_f32_16x16x32_bf16 v[72:75], v[184:187], v[208:211], v[72:75]
	v_mfma_f32_16x16x32_bf16 v[68:71], v[176:179], v[216:219], v[68:71]
	v_mfma_f32_16x16x32_bf16 v[64:67], v[184:187], v[216:219], v[64:67]
	v_mfma_f32_16x16x32_bf16 v[92:95], v[180:183], v[196:199], v[92:95]
	v_mfma_f32_16x16x32_bf16 v[88:91], v[188:191], v[196:199], v[88:91]
	v_mfma_f32_16x16x32_bf16 v[84:87], v[180:183], v[204:207], v[84:87]
	v_mfma_f32_16x16x32_bf16 v[80:83], v[188:191], v[204:207], v[80:83]
	v_mfma_f32_16x16x32_bf16 v[76:79], v[180:183], v[212:215], v[76:79]
	v_mfma_f32_16x16x32_bf16 v[72:75], v[188:191], v[212:215], v[72:75]
	v_mfma_f32_16x16x32_bf16 v[68:71], v[180:183], v[220:223], v[68:71]
	v_mfma_f32_16x16x32_bf16 v[64:67], v[188:191], v[220:223], v[64:67]
	s_setprio 0
	s_barrier
	s_mov_b32 m0, s34
	v_lshl_add_u64 v[224:225], s[26:27], 0, v[128:129]
	s_add_u32 s56, s26, 0x100000
	ds_read_b128 v[192:195], v158 offset:16384
	ds_read_b128 v[196:199], v158 offset:17408
	ds_read_b128 v[200:203], v158 offset:18432
	ds_read_b128 v[204:207], v158 offset:19456
	ds_read_b128 v[208:211], v158 offset:20480
	ds_read_b128 v[212:215], v158 offset:21504
	ds_read_b128 v[216:219], v158 offset:22528
	ds_read_b128 v[220:223], v158 offset:23552
	global_load_lds_dwordx4 v[224:225], off
	v_lshl_add_u64 v[226:227], s[26:27], 0, v[130:131]
	s_mov_b32 m0, s35
	s_addc_u32 s57, s27, 0
	global_load_lds_dwordx4 v[226:227], off
	s_mov_b32 m0, s36
	s_nop 0
	global_load_lds_dwordx4 v128, s[56:57]
	s_mov_b32 m0, s37
	s_nop 0
	global_load_lds_dwordx4 v130, s[56:57]
	s_waitcnt vmcnt(6)
	s_waitcnt lgkmcnt(0)
	s_barrier
	s_setprio 1
	s_waitcnt lgkmcnt(0)
	v_mfma_f32_16x16x32_bf16 v[60:63], v[160:163], v[192:195], v[60:63]
	v_mfma_f32_16x16x32_bf16 v[56:59], v[168:171], v[192:195], v[56:59]
	v_mfma_f32_16x16x32_bf16 v[52:55], v[160:163], v[200:203], v[52:55]
	v_mfma_f32_16x16x32_bf16 v[48:51], v[168:171], v[200:203], v[48:51]
	v_mfma_f32_16x16x32_bf16 v[44:47], v[160:163], v[208:211], v[44:47]
	v_mfma_f32_16x16x32_bf16 v[40:43], v[168:171], v[208:211], v[40:43]
	v_mfma_f32_16x16x32_bf16 v[36:39], v[160:163], v[216:219], v[36:39]
	v_mfma_f32_16x16x32_bf16 v[32:35], v[168:171], v[216:219], v[32:35]
	v_mfma_f32_16x16x32_bf16 v[60:63], v[164:167], v[196:199], v[60:63]
	v_mfma_f32_16x16x32_bf16 v[56:59], v[172:175], v[196:199], v[56:59]
	v_mfma_f32_16x16x32_bf16 v[52:55], v[164:167], v[204:207], v[52:55]
	v_mfma_f32_16x16x32_bf16 v[48:51], v[172:175], v[204:207], v[48:51]
	v_mfma_f32_16x16x32_bf16 v[44:47], v[164:167], v[212:215], v[44:47]
	v_mfma_f32_16x16x32_bf16 v[40:43], v[172:175], v[212:215], v[40:43]
	v_mfma_f32_16x16x32_bf16 v[36:39], v[164:167], v[220:223], v[36:39]
	v_mfma_f32_16x16x32_bf16 v[32:35], v[172:175], v[220:223], v[32:35]
	s_setprio 0
	s_setprio 1
	v_mfma_f32_16x16x32_bf16 v[28:31], v[176:179], v[192:195], v[28:31]
	v_mfma_f32_16x16x32_bf16 v[24:27], v[184:187], v[192:195], v[24:27]
	v_mfma_f32_16x16x32_bf16 v[20:23], v[176:179], v[200:203], v[20:23]
	v_mfma_f32_16x16x32_bf16 v[16:19], v[184:187], v[200:203], v[16:19]
	v_mfma_f32_16x16x32_bf16 v[12:15], v[176:179], v[208:211], v[12:15]
	v_mfma_f32_16x16x32_bf16 v[8:11], v[184:187], v[208:211], v[8:11]
	v_mfma_f32_16x16x32_bf16 v[4:7], v[176:179], v[216:219], v[4:7]
	v_mfma_f32_16x16x32_bf16 v[0:3], v[184:187], v[216:219], v[0:3]
	v_mfma_f32_16x16x32_bf16 v[28:31], v[180:183], v[196:199], v[28:31]
	v_mfma_f32_16x16x32_bf16 v[24:27], v[188:191], v[196:199], v[24:27]
	v_mfma_f32_16x16x32_bf16 v[20:23], v[180:183], v[204:207], v[20:23]
	v_mfma_f32_16x16x32_bf16 v[16:19], v[188:191], v[204:207], v[16:19]
	v_mfma_f32_16x16x32_bf16 v[12:15], v[180:183], v[212:215], v[12:15]
	v_mfma_f32_16x16x32_bf16 v[8:11], v[188:191], v[212:215], v[8:11]
	v_mfma_f32_16x16x32_bf16 v[4:7], v[180:183], v[220:223], v[4:7]
	v_mfma_f32_16x16x32_bf16 v[0:3], v[188:191], v[220:223], v[0:3]
	s_setprio 0
	s_barrier
	s_mov_b32 m0, s33
	s_nop 0
	global_load_lds_dwordx4 v128, s[28:29]
	s_mov_b32 m0, s38
	s_nop 0
	global_load_lds_dwordx4 v130, s[28:29]
	ds_read_b128 v[160:163], v150
	ds_read_b128 v[164:167], v151
	ds_read_b128 v[168:171], v152
	ds_read_b128 v[172:175], v153
	ds_read_b128 v[176:179], v154
	ds_read_b128 v[180:183], v155
	ds_read_b128 v[184:187], v156
	ds_read_b128 v[188:191], v157
	s_add_u32 s28, s28, 0x100000
	s_addc_u32 s29, s29, 0
	s_mov_b32 m0, s39
	ds_read_b128 v[192:195], v158 offset:32768
	ds_read_b128 v[196:199], v158 offset:33792
	ds_read_b128 v[200:203], v158 offset:34816
	ds_read_b128 v[204:207], v158 offset:35840
	ds_read_b128 v[208:211], v158 offset:36864
	ds_read_b128 v[212:215], v158 offset:37888
	ds_read_b128 v[216:219], v158 offset:38912
	ds_read_b128 v[220:223], v158 offset:39936
	global_load_lds_dwordx4 v128, s[28:29]
	s_mov_b32 m0, s40
	s_nop 0
	global_load_lds_dwordx4 v130, s[28:29]
	s_waitcnt vmcnt(8)
	s_waitcnt lgkmcnt(0)
	s_barrier
	s_setprio 1
	s_waitcnt lgkmcnt(0)
	v_mfma_f32_16x16x32_bf16 v[124:127], v[160:163], v[192:195], v[124:127]
	v_mfma_f32_16x16x32_bf16 v[120:123], v[168:171], v[192:195], v[120:123]
	v_mfma_f32_16x16x32_bf16 v[116:119], v[160:163], v[200:203], v[116:119]
	v_mfma_f32_16x16x32_bf16 v[112:115], v[168:171], v[200:203], v[112:115]
	v_mfma_f32_16x16x32_bf16 v[108:111], v[160:163], v[208:211], v[108:111]
	v_mfma_f32_16x16x32_bf16 v[104:107], v[168:171], v[208:211], v[104:107]
	v_mfma_f32_16x16x32_bf16 v[100:103], v[160:163], v[216:219], v[100:103]
	v_mfma_f32_16x16x32_bf16 v[96:99], v[168:171], v[216:219], v[96:99]
	v_mfma_f32_16x16x32_bf16 v[124:127], v[164:167], v[196:199], v[124:127]
	v_mfma_f32_16x16x32_bf16 v[120:123], v[172:175], v[196:199], v[120:123]
	v_mfma_f32_16x16x32_bf16 v[116:119], v[164:167], v[204:207], v[116:119]
	v_mfma_f32_16x16x32_bf16 v[112:115], v[172:175], v[204:207], v[112:115]
	v_mfma_f32_16x16x32_bf16 v[108:111], v[164:167], v[212:215], v[108:111]
	v_mfma_f32_16x16x32_bf16 v[104:107], v[172:175], v[212:215], v[104:107]
	v_mfma_f32_16x16x32_bf16 v[100:103], v[164:167], v[220:223], v[100:103]
	v_mfma_f32_16x16x32_bf16 v[96:99], v[172:175], v[220:223], v[96:99]
	s_setprio 0
	s_setprio 1
	v_mfma_f32_16x16x32_bf16 v[92:95], v[176:179], v[192:195], v[92:95]
	v_mfma_f32_16x16x32_bf16 v[88:91], v[184:187], v[192:195], v[88:91]
	v_mfma_f32_16x16x32_bf16 v[84:87], v[176:179], v[200:203], v[84:87]
	v_mfma_f32_16x16x32_bf16 v[80:83], v[184:187], v[200:203], v[80:83]
	v_mfma_f32_16x16x32_bf16 v[76:79], v[176:179], v[208:211], v[76:79]
	v_mfma_f32_16x16x32_bf16 v[72:75], v[184:187], v[208:211], v[72:75]
	v_mfma_f32_16x16x32_bf16 v[68:71], v[176:179], v[216:219], v[68:71]
	v_mfma_f32_16x16x32_bf16 v[64:67], v[184:187], v[216:219], v[64:67]
	v_mfma_f32_16x16x32_bf16 v[92:95], v[180:183], v[196:199], v[92:95]
	v_mfma_f32_16x16x32_bf16 v[88:91], v[188:191], v[196:199], v[88:91]
	v_mfma_f32_16x16x32_bf16 v[84:87], v[180:183], v[204:207], v[84:87]
	v_mfma_f32_16x16x32_bf16 v[80:83], v[188:191], v[204:207], v[80:83]
	v_mfma_f32_16x16x32_bf16 v[76:79], v[180:183], v[212:215], v[76:79]
	v_mfma_f32_16x16x32_bf16 v[72:75], v[188:191], v[212:215], v[72:75]
	v_mfma_f32_16x16x32_bf16 v[68:71], v[180:183], v[220:223], v[68:71]
	v_mfma_f32_16x16x32_bf16 v[64:67], v[188:191], v[220:223], v[64:67]
	s_setprio 0
	s_barrier
	s_mov_b32 m0, s42
	v_lshl_add_u64 v[224:225], v[224:225], 0, s[10:11]
	s_add_u32 s26, s26, 0x100080
	ds_read_b128 v[192:195], v158 offset:49152
	ds_read_b128 v[196:199], v158 offset:50176
	ds_read_b128 v[200:203], v158 offset:51200
	ds_read_b128 v[204:207], v158 offset:52224
	ds_read_b128 v[208:211], v158 offset:53248
	ds_read_b128 v[212:215], v158 offset:54272
	ds_read_b128 v[216:219], v158 offset:55296
	ds_read_b128 v[220:223], v158 offset:56320
	global_load_lds_dwordx4 v[224:225], off
	v_lshl_add_u64 v[224:225], v[226:227], 0, s[10:11]
	s_mov_b32 m0, s43
	s_addc_u32 s27, s27, 0
	global_load_lds_dwordx4 v[224:225], off
	s_mov_b32 m0, s46
	s_nop 0
	global_load_lds_dwordx4 v128, s[26:27]
	s_mov_b32 m0, s47
	s_nop 0
	global_load_lds_dwordx4 v130, s[26:27]
	s_waitcnt vmcnt(6)
	s_waitcnt lgkmcnt(0)
	s_barrier
	s_setprio 1
	s_waitcnt lgkmcnt(0)
	v_mfma_f32_16x16x32_bf16 v[60:63], v[160:163], v[192:195], v[60:63]
	v_mfma_f32_16x16x32_bf16 v[56:59], v[168:171], v[192:195], v[56:59]
	v_mfma_f32_16x16x32_bf16 v[52:55], v[160:163], v[200:203], v[52:55]
	v_mfma_f32_16x16x32_bf16 v[48:51], v[168:171], v[200:203], v[48:51]
	v_mfma_f32_16x16x32_bf16 v[44:47], v[160:163], v[208:211], v[44:47]
	v_mfma_f32_16x16x32_bf16 v[40:43], v[168:171], v[208:211], v[40:43]
	v_mfma_f32_16x16x32_bf16 v[36:39], v[160:163], v[216:219], v[36:39]
	v_mfma_f32_16x16x32_bf16 v[32:35], v[168:171], v[216:219], v[32:35]
	v_mfma_f32_16x16x32_bf16 v[60:63], v[164:167], v[196:199], v[60:63]
	v_mfma_f32_16x16x32_bf16 v[56:59], v[172:175], v[196:199], v[56:59]
	v_mfma_f32_16x16x32_bf16 v[52:55], v[164:167], v[204:207], v[52:55]
	v_mfma_f32_16x16x32_bf16 v[48:51], v[172:175], v[204:207], v[48:51]
	v_mfma_f32_16x16x32_bf16 v[44:47], v[164:167], v[212:215], v[44:47]
	v_mfma_f32_16x16x32_bf16 v[40:43], v[172:175], v[212:215], v[40:43]
	v_mfma_f32_16x16x32_bf16 v[36:39], v[164:167], v[220:223], v[36:39]
	v_mfma_f32_16x16x32_bf16 v[32:35], v[172:175], v[220:223], v[32:35]
	s_setprio 0
	s_setprio 1
	v_mfma_f32_16x16x32_bf16 v[28:31], v[176:179], v[192:195], v[28:31]
	v_mfma_f32_16x16x32_bf16 v[24:27], v[184:187], v[192:195], v[24:27]
	v_mfma_f32_16x16x32_bf16 v[20:23], v[176:179], v[200:203], v[20:23]
	v_mfma_f32_16x16x32_bf16 v[16:19], v[184:187], v[200:203], v[16:19]
	v_mfma_f32_16x16x32_bf16 v[12:15], v[176:179], v[208:211], v[12:15]
	v_mfma_f32_16x16x32_bf16 v[8:11], v[184:187], v[208:211], v[8:11]
	v_mfma_f32_16x16x32_bf16 v[4:7], v[176:179], v[216:219], v[4:7]
	v_mfma_f32_16x16x32_bf16 v[0:3], v[184:187], v[216:219], v[0:3]
	v_mfma_f32_16x16x32_bf16 v[28:31], v[180:183], v[196:199], v[28:31]
	v_mfma_f32_16x16x32_bf16 v[24:27], v[188:191], v[196:199], v[24:27]
	v_mfma_f32_16x16x32_bf16 v[20:23], v[180:183], v[204:207], v[20:23]
	v_mfma_f32_16x16x32_bf16 v[16:19], v[188:191], v[204:207], v[16:19]
	v_mfma_f32_16x16x32_bf16 v[12:15], v[180:183], v[212:215], v[12:15]
	v_mfma_f32_16x16x32_bf16 v[8:11], v[188:191], v[212:215], v[8:11]
	v_mfma_f32_16x16x32_bf16 v[4:7], v[180:183], v[220:223], v[4:7]
	v_mfma_f32_16x16x32_bf16 v[0:3], v[188:191], v[220:223], v[0:3]
	s_add_i32 s54, s54, 2
	s_add_u32 s24, s24, 0x100
	s_addc_u32 s25, s25, 0
	s_add_u32 s52, s52, 0x100
	s_addc_u32 s53, s53, 0
	s_setprio 0
	s_barrier
	s_cmp_gt_u32 s54, 61
	s_cbranch_scc0 .LBB0_687
	s_and_b64 vcc, exec, s[12:13]
	s_cbranch_vccz .LBB0_690
	s_barrier

.Lp8s_63:
	s_add_i32 s64, s64, 2
	s_add_u32 s38, s38, 0x100
	s_addc_u32 s39, s39, 0
	s_add_u32 s60, s60, 0x100
	s_addc_u32 s61, s61, 0
	s_setprio 0
	s_barrier
	s_cmp_gt_u32 s64, 29
	s_cbranch_scc0 .LBB0_940
	s_nop 15
	s_nop 15
	s_and_b64 vcc, exec, s[14:15]
	s_cbranch_vccz .LBB0_943
	s_barrier

.LBB0_1358:
	s_add_u32 s30, s26, 0x1000
	s_addc_u32 s31, s27, 0
	s_mov_b32 m0, s49
	s_nop 0
	global_load_lds_dwordx4 v160, s[30:31]
	s_mov_b32 m0, s50
	s_nop 0
	global_load_lds_dwordx4 v164, s[30:31]
	ds_read_b128 v[16:19], v207
	ds_read_b128 v[20:23], v208
	ds_read_b128 v[24:27], v209
	ds_read_b128 v[28:31], v210
	ds_read_b128 v[0:3], v211
	ds_read_b128 v[4:7], v212
	ds_read_b128 v[8:11], v213
	ds_read_b128 v[12:15], v214
	s_add_u32 s28, s26, 0x10000
	s_addc_u32 s29, s27, 0
	s_cmpk_eq_i32 s59, 0x7c
	s_cselect_b32 s36, s55, s28
	s_cselect_b32 s37, s19, s29
	s_cselect_b32 s34, s56, s57
	s_cselect_b32 s35, s17, s58
	s_add_i32 m0, s25, 0xc000
	ds_read_b128 v[176:179], v224
	ds_read_b128 v[180:183], v224 offset:1024
	ds_read_b128 v[184:187], v224 offset:2048
	ds_read_b128 v[188:191], v224 offset:3072
	ds_read_b128 v[192:195], v224 offset:4096
	ds_read_b128 v[196:199], v224 offset:5120
	ds_read_b128 v[226:229], v224 offset:6144
	ds_read_b128 v[230:233], v224 offset:7168
	global_load_lds_dwordx4 v168, s[26:27]
	s_add_i32 m0, s25, 0xe000
	s_nop 0
	global_load_lds_dwordx4 v170, s[26:27]
	s_waitcnt vmcnt(8)
	s_waitcnt lgkmcnt(0)
	s_barrier
	s_setprio 1
	s_waitcnt lgkmcnt(0)
	v_mfma_f32_16x16x128_f8f6f4 v[156:159], v[16:23], v[176:183], v[156:159]
	v_mfma_f32_16x16x128_f8f6f4 v[152:155], v[24:31], v[176:183], v[152:155]
	v_mfma_f32_16x16x128_f8f6f4 v[144:147], v[16:23], v[184:191], v[144:147]
	v_mfma_f32_16x16x128_f8f6f4 v[136:139], v[24:31], v[184:191], v[136:139]
	v_mfma_f32_16x16x128_f8f6f4 v[124:127], v[16:23], v[192:199], v[124:127]
	v_mfma_f32_16x16x128_f8f6f4 v[120:123], v[24:31], v[192:199], v[120:123]
	v_mfma_f32_16x16x128_f8f6f4 v[112:115], v[16:23], v[226:233], v[112:115]
	v_mfma_f32_16x16x128_f8f6f4 v[104:107], v[24:31], v[226:233], v[104:107]
	s_setprio 0
	s_setprio 1
	v_mfma_f32_16x16x128_f8f6f4 v[148:151], v[0:7], v[176:183], v[148:151]
	v_mfma_f32_16x16x128_f8f6f4 v[140:143], v[8:15], v[176:183], v[140:143]
	v_mfma_f32_16x16x128_f8f6f4 v[132:135], v[0:7], v[184:191], v[132:135]
	v_mfma_f32_16x16x128_f8f6f4 v[128:131], v[8:15], v[184:191], v[128:131]
	v_mfma_f32_16x16x128_f8f6f4 v[116:119], v[0:7], v[192:199], v[116:119]
	v_mfma_f32_16x16x128_f8f6f4 v[108:111], v[8:15], v[192:199], v[108:111]
	v_mfma_f32_16x16x128_f8f6f4 v[100:103], v[0:7], v[226:233], v[100:103]
	v_mfma_f32_16x16x128_f8f6f4 v[96:99], v[8:15], v[226:233], v[96:99]
	s_setprio 0
	s_barrier
	s_mov_b32 m0, s33
	v_lshl_add_u64 v[176:177], s[34:35], 0, v[162:163]
	s_add_u32 s26, s34, 0x200000
	ds_read_b128 v[180:183], v224 offset:16384
	ds_read_b128 v[184:187], v224 offset:17408
	ds_read_b128 v[188:191], v224 offset:18432
	ds_read_b128 v[192:195], v224 offset:19456
	ds_read_b128 v[196:199], v224 offset:20480
	ds_read_b128 v[200:203], v224 offset:21504
	ds_read_b128 v[226:229], v224 offset:22528
	ds_read_b128 v[230:233], v224 offset:23552
	global_load_lds_dwordx4 v[176:177], off
	v_lshl_add_u64 v[178:179], s[34:35], 0, v[166:167]
	s_mov_b32 m0, s38
	s_addc_u32 s27, s35, 0
	global_load_lds_dwordx4 v[178:179], off
	s_mov_b32 m0, s39
	s_nop 0
	global_load_lds_dwordx4 v162, s[26:27]
	s_mov_b32 m0, s40
	s_nop 0
	global_load_lds_dwordx4 v166, s[26:27]
	s_waitcnt vmcnt(6)
	s_waitcnt lgkmcnt(0)
	s_barrier
	s_setprio 1
	s_waitcnt lgkmcnt(0)
	v_mfma_f32_16x16x128_f8f6f4 v[92:95], v[16:23], v[180:187], v[92:95]
	v_mfma_f32_16x16x128_f8f6f4 v[88:91], v[24:31], v[180:187], v[88:91]
	v_mfma_f32_16x16x128_f8f6f4 v[80:83], v[16:23], v[188:195], v[80:83]
	v_mfma_f32_16x16x128_f8f6f4 v[72:75], v[24:31], v[188:195], v[72:75]
	v_mfma_f32_16x16x128_f8f6f4 v[64:67], v[16:23], v[196:203], v[64:67]
	v_mfma_f32_16x16x128_f8f6f4 v[56:59], v[24:31], v[196:203], v[56:59]
	v_mfma_f32_16x16x128_f8f6f4 v[48:51], v[16:23], v[226:233], v[48:51]
	v_mfma_f32_16x16x128_f8f6f4 v[40:43], v[24:31], v[226:233], v[40:43]
	s_setprio 0
	s_setprio 1
	v_mfma_f32_16x16x128_f8f6f4 v[84:87], v[0:7], v[180:187], v[84:87]
	v_mfma_f32_16x16x128_f8f6f4 v[76:79], v[8:15], v[180:187], v[76:79]
	v_mfma_f32_16x16x128_f8f6f4 v[68:71], v[0:7], v[188:195], v[68:71]
	v_mfma_f32_16x16x128_f8f6f4 v[60:63], v[8:15], v[188:195], v[60:63]
	v_mfma_f32_16x16x128_f8f6f4 v[52:55], v[0:7], v[196:203], v[52:55]
	v_mfma_f32_16x16x128_f8f6f4 v[44:47], v[8:15], v[196:203], v[44:47]
	v_mfma_f32_16x16x128_f8f6f4 v[36:39], v[0:7], v[226:233], v[36:39]
	v_mfma_f32_16x16x128_f8f6f4 v[32:35], v[8:15], v[226:233], v[32:35]
	s_setprio 0
	s_barrier
	s_mov_b32 m0, s25
	s_nop 0
	global_load_lds_dwordx4 v160, s[36:37]
	s_mov_b32 m0, s41
	s_nop 0
	global_load_lds_dwordx4 v164, s[36:37]
	ds_read_b128 v[0:3], v215
	ds_read_b128 v[4:7], v216
	ds_read_b128 v[8:11], v217
	ds_read_b128 v[12:15], v218
	ds_read_b128 v[16:19], v219
	ds_read_b128 v[20:23], v220
	ds_read_b128 v[24:27], v221
	ds_read_b128 v[28:31], v222
	s_add_u32 s26, s36, 0x8000
	s_addc_u32 s27, s37, 0
	s_mov_b32 m0, s42
	ds_read_b128 v[180:183], v224 offset:32768
	ds_read_b128 v[184:187], v224 offset:33792
	ds_read_b128 v[188:191], v224 offset:34816
	ds_read_b128 v[192:195], v224 offset:35840
	ds_read_b128 v[196:199], v224 offset:36864
	ds_read_b128 v[200:203], v224 offset:37888
	ds_read_b128 v[226:229], v224 offset:38912
	ds_read_b128 v[230:233], v224 offset:39936
	global_load_lds_dwordx4 v160, s[26:27]
	s_mov_b32 m0, s43
	s_nop 0
	global_load_lds_dwordx4 v164, s[26:27]
	s_waitcnt vmcnt(8)
	s_waitcnt lgkmcnt(0)
	s_barrier
	s_setprio 1
	s_waitcnt lgkmcnt(0)
	v_mfma_f32_16x16x128_f8f6f4 v[156:159], v[0:7], v[180:187], v[156:159]
	v_mfma_f32_16x16x128_f8f6f4 v[152:155], v[8:15], v[180:187], v[152:155]
	v_mfma_f32_16x16x128_f8f6f4 v[144:147], v[0:7], v[188:195], v[144:147]
	v_mfma_f32_16x16x128_f8f6f4 v[136:139], v[8:15], v[188:195], v[136:139]
	v_mfma_f32_16x16x128_f8f6f4 v[124:127], v[0:7], v[196:203], v[124:127]
	v_mfma_f32_16x16x128_f8f6f4 v[120:123], v[8:15], v[196:203], v[120:123]
	v_mfma_f32_16x16x128_f8f6f4 v[112:115], v[0:7], v[226:233], v[112:115]
	v_mfma_f32_16x16x128_f8f6f4 v[104:107], v[8:15], v[226:233], v[104:107]
	s_setprio 0
	s_setprio 1
	v_mfma_f32_16x16x128_f8f6f4 v[148:151], v[16:23], v[180:187], v[148:151]
	v_mfma_f32_16x16x128_f8f6f4 v[140:143], v[24:31], v[180:187], v[140:143]
	v_mfma_f32_16x16x128_f8f6f4 v[132:135], v[16:23], v[188:195], v[132:135]
	v_mfma_f32_16x16x128_f8f6f4 v[128:131], v[24:31], v[188:195], v[128:131]
	v_mfma_f32_16x16x128_f8f6f4 v[116:119], v[16:23], v[196:203], v[116:119]
	v_mfma_f32_16x16x128_f8f6f4 v[108:111], v[24:31], v[196:203], v[108:111]
	v_mfma_f32_16x16x128_f8f6f4 v[100:103], v[16:23], v[226:233], v[100:103]
	v_mfma_f32_16x16x128_f8f6f4 v[96:99], v[24:31], v[226:233], v[96:99]
	s_setprio 0
	s_barrier
	s_mov_b32 m0, s47
	v_lshl_add_u64 v[176:177], v[176:177], 0, s[10:11]
	s_add_u32 s26, s34, 0x200080
	ds_read_b128 v[180:183], v224 offset:49152
	ds_read_b128 v[184:187], v224 offset:50176
	ds_read_b128 v[188:191], v224 offset:51200
	ds_read_b128 v[192:195], v224 offset:52224
	ds_read_b128 v[196:199], v224 offset:53248
	ds_read_b128 v[200:203], v224 offset:54272
	ds_read_b128 v[226:229], v224 offset:55296
	ds_read_b128 v[230:233], v224 offset:56320
	global_load_lds_dwordx4 v[176:177], off
	v_lshl_add_u64 v[176:177], v[178:179], 0, s[10:11]
	s_mov_b32 m0, s48
	s_addc_u32 s27, s35, 0
	global_load_lds_dwordx4 v[176:177], off
	s_mov_b32 m0, s51
	s_nop 0
	global_load_lds_dwordx4 v162, s[26:27]
	s_mov_b32 m0, s52
	s_nop 0
	global_load_lds_dwordx4 v166, s[26:27]
	s_waitcnt vmcnt(6)
	s_waitcnt lgkmcnt(0)
	s_barrier
	s_setprio 1
	s_waitcnt lgkmcnt(0)
	v_mfma_f32_16x16x128_f8f6f4 v[92:95], v[0:7], v[180:187], v[92:95]
	v_mfma_f32_16x16x128_f8f6f4 v[88:91], v[8:15], v[180:187], v[88:91]
	v_mfma_f32_16x16x128_f8f6f4 v[80:83], v[0:7], v[188:195], v[80:83]
	v_mfma_f32_16x16x128_f8f6f4 v[72:75], v[8:15], v[188:195], v[72:75]
	v_mfma_f32_16x16x128_f8f6f4 v[64:67], v[0:7], v[196:203], v[64:67]
	v_mfma_f32_16x16x128_f8f6f4 v[56:59], v[8:15], v[196:203], v[56:59]
	v_mfma_f32_16x16x128_f8f6f4 v[48:51], v[0:7], v[226:233], v[48:51]
	v_mfma_f32_16x16x128_f8f6f4 v[40:43], v[8:15], v[226:233], v[40:43]
	s_setprio 0
	s_setprio 1
	v_mfma_f32_16x16x128_f8f6f4 v[84:87], v[16:23], v[180:187], v[84:87]
	v_mfma_f32_16x16x128_f8f6f4 v[76:79], v[24:31], v[180:187], v[76:79]
	v_mfma_f32_16x16x128_f8f6f4 v[68:71], v[16:23], v[188:195], v[68:71]
	v_mfma_f32_16x16x128_f8f6f4 v[60:63], v[24:31], v[188:195], v[60:63]
	v_mfma_f32_16x16x128_f8f6f4 v[52:55], v[16:23], v[196:203], v[52:55]
	v_mfma_f32_16x16x128_f8f6f4 v[44:47], v[24:31], v[196:203], v[44:47]
	v_mfma_f32_16x16x128_f8f6f4 v[36:39], v[16:23], v[226:233], v[36:39]
	v_mfma_f32_16x16x128_f8f6f4 v[32:35], v[24:31], v[226:233], v[32:35]
	s_add_i32 s59, s59, 2
	s_add_u32 s57, s57, 0x100
	s_addc_u32 s58, s58, 0
	s_mov_b64 s[26:27], s[28:29]
	s_setprio 0
	s_barrier
	s_cmpk_gt_u32 s59, 0x7d
	s_cbranch_scc0 .LBB0_1358
	s_nop 15
	s_nop 15
	s_and_b64 vcc, exec, s[12:13]
	s_cbranch_vccz .LBB0_1361
	s_barrier
